# v10 + up GEMM: accumulators re-zeroed inside the hand-written epilogue (loop-top zeroing skipped for units after the first)
# baseline (speedup 1.0000x reference)
.LBB0_1884:
	s_ashr_i32 s25, s24, 31
	s_lshl_b64 s[26:27], s[24:25], 19
	s_add_u32 s26, s60, s26
	s_addc_u32 s27, s61, s27
	s_and_b64 s[28:29], s[4:5], exec
	s_cselect_b32 s25, s27, s39
	s_cselect_b32 s33, s26, s38
	s_ashr_i32 s23, s22, 31
	s_lshl_b64 s[28:29], s[22:23], 19
	s_add_u32 s28, s54, s28
	s_addc_u32 s29, s55, s29
	s_and_b64 s[68:69], s[4:5], exec
	s_cselect_b32 s23, s29, s37
	s_cselect_b32 s94, s28, s36
	v_mov_b32_e32 v2, 0
	s_cmp_lt_i32 s22, 4
	s_mov_b32 s95, 0
	s_cselect_b64 s[68:69], -1, 0
	s_cmp_lg_u32 s85, 1
	s_cbranch_scc1 .Lup_skipzero
	v_mov_b32_e32 v3, v2
	v_mov_b32_e32 v4, v2
	v_mov_b32_e32 v5, v2
	v_mov_b32_e32 v6, v2
	v_mov_b32_e32 v7, v2
	v_mov_b32_e32 v8, v2
	v_mov_b32_e32 v9, v2
	v_mov_b32_e32 v18, v2
	v_mov_b32_e32 v19, v2
	v_mov_b32_e32 v20, v2
	v_mov_b32_e32 v21, v2
	v_mov_b32_e32 v22, v2
	v_mov_b32_e32 v23, v2
	v_mov_b32_e32 v24, v2
	v_mov_b32_e32 v25, v2
	v_mov_b32_e32 v34, v2
	v_mov_b32_e32 v35, v2
	v_mov_b32_e32 v36, v2
	v_mov_b32_e32 v37, v2
	v_mov_b32_e32 v38, v2
	v_mov_b32_e32 v39, v2
	v_mov_b32_e32 v40, v2
	v_mov_b32_e32 v41, v2
	v_mov_b32_e32 v50, v2
	v_mov_b32_e32 v51, v2
	v_mov_b32_e32 v52, v2
	v_mov_b32_e32 v53, v2
	v_mov_b32_e32 v54, v2
	v_mov_b32_e32 v55, v2
	v_mov_b32_e32 v56, v2
	v_mov_b32_e32 v57, v2
	v_mov_b32_e32 v10, v2
	v_mov_b32_e32 v11, v2
	v_mov_b32_e32 v12, v2
	v_mov_b32_e32 v13, v2
	v_mov_b32_e32 v14, v2
	v_mov_b32_e32 v15, v2
	v_mov_b32_e32 v16, v2
	v_mov_b32_e32 v17, v2
	v_mov_b32_e32 v26, v2
	v_mov_b32_e32 v27, v2
	v_mov_b32_e32 v28, v2
	v_mov_b32_e32 v29, v2
	v_mov_b32_e32 v30, v2
	v_mov_b32_e32 v31, v2
	v_mov_b32_e32 v32, v2
	v_mov_b32_e32 v33, v2
	v_mov_b32_e32 v42, v2
	v_mov_b32_e32 v43, v2
	v_mov_b32_e32 v44, v2
	v_mov_b32_e32 v45, v2
	v_mov_b32_e32 v46, v2
	v_mov_b32_e32 v47, v2
	v_mov_b32_e32 v48, v2
	v_mov_b32_e32 v49, v2
	v_mov_b32_e32 v58, v2
	v_mov_b32_e32 v59, v2
	v_mov_b32_e32 v60, v2
	v_mov_b32_e32 v61, v2
	v_mov_b32_e32 v62, v2
	v_mov_b32_e32 v63, v2
	v_mov_b32_e32 v64, v2
	v_mov_b32_e32 v65, v2
	v_mov_b32_e32 v66, v2
	v_mov_b32_e32 v67, v2
	v_mov_b32_e32 v68, v2
	v_mov_b32_e32 v69, v2
	v_mov_b32_e32 v70, v2
	v_mov_b32_e32 v71, v2
	v_mov_b32_e32 v72, v2
	v_mov_b32_e32 v73, v2
	v_mov_b32_e32 v82, v2
	v_mov_b32_e32 v83, v2
	v_mov_b32_e32 v84, v2
	v_mov_b32_e32 v85, v2
	v_mov_b32_e32 v86, v2
	v_mov_b32_e32 v87, v2
	v_mov_b32_e32 v88, v2
	v_mov_b32_e32 v89, v2
	v_mov_b32_e32 v98, v2
	v_mov_b32_e32 v99, v2
	v_mov_b32_e32 v100, v2
	v_mov_b32_e32 v101, v2
	v_mov_b32_e32 v102, v2
	v_mov_b32_e32 v103, v2
	v_mov_b32_e32 v104, v2
	v_mov_b32_e32 v105, v2
	v_mov_b32_e32 v114, v2
	v_mov_b32_e32 v115, v2
	v_mov_b32_e32 v116, v2
	v_mov_b32_e32 v117, v2
	v_mov_b32_e32 v118, v2
	v_mov_b32_e32 v119, v2
	v_mov_b32_e32 v120, v2
	v_mov_b32_e32 v121, v2
	v_mov_b32_e32 v74, v2
	v_mov_b32_e32 v75, v2
	v_mov_b32_e32 v76, v2
	v_mov_b32_e32 v77, v2
	v_mov_b32_e32 v78, v2
	v_mov_b32_e32 v79, v2
	v_mov_b32_e32 v80, v2
	v_mov_b32_e32 v81, v2
	v_mov_b32_e32 v90, v2
	v_mov_b32_e32 v91, v2
	v_mov_b32_e32 v92, v2
	v_mov_b32_e32 v93, v2
	v_mov_b32_e32 v94, v2
	v_mov_b32_e32 v95, v2
	v_mov_b32_e32 v96, v2
	v_mov_b32_e32 v97, v2
	v_mov_b32_e32 v106, v2
	v_mov_b32_e32 v107, v2
	v_mov_b32_e32 v108, v2
	v_mov_b32_e32 v109, v2
	v_mov_b32_e32 v110, v2
	v_mov_b32_e32 v111, v2
	v_mov_b32_e32 v112, v2
	v_mov_b32_e32 v113, v2
	v_mov_b32_e32 v122, v2
	v_mov_b32_e32 v123, v2
	v_mov_b32_e32 v124, v2
	v_mov_b32_e32 v125, v2
	v_mov_b32_e32 v126, v2
	v_mov_b32_e32 v127, v2
	v_mov_b32_e32 v128, v2
	v_mov_b32_e32 v129, v2
.Lup_skipzero:
	s_branch .LBB0_1889
.LBB0_1885:
	s_or_b64 exec, exec, s[74:75]

.LBB0_1914:
.LBB0_1915:
	v_lshrrev_b32_e32 v149, 2, v248
	v_and_b32_e32 v150, 3, v248
	v_lshlrev_b32_e32 v148, 6, v150
	v_lshl_add_u32 v148, v149, 2, v148
	v_and_b32_e32 v151, -16, v1
	v_or_b32_e32 v151, v151, v149
	v_lshl_add_u32 v151, s34, 8, v151
	v_and_b32_e32 v152, 0x60, v145
	v_lshl_or_b32 v152, v150, 3, v152
	v_lshl_or_b32 v152, s30, 8, v152
	v_lshlrev_b32_e32 v142, 13, v151
	v_lshl_add_u32 v142, v152, 1, v142
	v_mov_b32_e32 v143, 0
	s_mov_b32 s98, 0x20000
	s_mov_b32 s99, 0
	s_mov_b32 s100, 0xa0000
	s_mov_b32 s101, 0
	v_lshl_add_u64 v[142:143], s[66:67], 0, v[142:143]
	v_max_f32_e32 v126, 0, v126
	v_max_f32_e32 v127, 0, v127
	v_max_f32_e32 v128, 0, v128
	v_max_f32_e32 v129, 0, v129
	v_max_f32_e32 v122, 0, v122
	v_max_f32_e32 v123, 0, v123
	v_max_f32_e32 v124, 0, v124
	v_max_f32_e32 v125, 0, v125
	v_mul_f32_e32 v126, v126, v126
	v_mul_f32_e32 v127, v127, v127
	v_mul_f32_e32 v128, v128, v128
	v_mul_f32_e32 v129, v129, v129
	v_mul_f32_e32 v122, v122, v122
	v_mul_f32_e32 v123, v123, v123
	v_mul_f32_e32 v124, v124, v124
	v_mul_f32_e32 v125, v125, v125
	v_cvt_pk_bf16_f32 v126, v126, v127
	v_cvt_pk_bf16_f32 v127, v128, v129
	v_cvt_pk_bf16_f32 v128, v122, v123
	v_cvt_pk_bf16_f32 v129, v124, v125
	ds_bpermute_b32 v126, v148, v126
	ds_bpermute_b32 v127, v148, v127
	ds_bpermute_b32 v128, v148, v128
	ds_bpermute_b32 v129, v148, v129
	v_mov_b32_e32 v122, 0
	v_mov_b32_e32 v123, 0
	v_mov_b32_e32 v124, 0
	v_mov_b32_e32 v125, 0
	v_max_f32_e32 v118, 0, v118
	v_max_f32_e32 v119, 0, v119
	v_max_f32_e32 v120, 0, v120
	v_max_f32_e32 v121, 0, v121
	v_max_f32_e32 v114, 0, v114
	v_max_f32_e32 v115, 0, v115
	v_max_f32_e32 v116, 0, v116
	v_max_f32_e32 v117, 0, v117
	v_mul_f32_e32 v118, v118, v118
	v_mul_f32_e32 v119, v119, v119
	v_mul_f32_e32 v120, v120, v120
	v_mul_f32_e32 v121, v121, v121
	v_mul_f32_e32 v114, v114, v114
	v_mul_f32_e32 v115, v115, v115
	v_mul_f32_e32 v116, v116, v116
	v_mul_f32_e32 v117, v117, v117
	v_cvt_pk_bf16_f32 v118, v118, v119
	v_cvt_pk_bf16_f32 v119, v120, v121
	v_cvt_pk_bf16_f32 v120, v114, v115
	v_cvt_pk_bf16_f32 v121, v116, v117
	ds_bpermute_b32 v118, v148, v118
	ds_bpermute_b32 v119, v148, v119
	ds_bpermute_b32 v120, v148, v120
	ds_bpermute_b32 v121, v148, v121
	v_mov_b32_e32 v114, 0
	v_mov_b32_e32 v115, 0
	v_mov_b32_e32 v116, 0
	v_mov_b32_e32 v117, 0
	s_waitcnt lgkmcnt(4)
	global_store_dwordx4 v[142:143], v[126:129], off
	v_max_f32_e32 v110, 0, v110
	v_max_f32_e32 v111, 0, v111
	v_max_f32_e32 v112, 0, v112
	v_max_f32_e32 v113, 0, v113
	v_max_f32_e32 v106, 0, v106
	v_max_f32_e32 v107, 0, v107
	v_max_f32_e32 v108, 0, v108
	v_max_f32_e32 v109, 0, v109
	v_mul_f32_e32 v110, v110, v110
	v_mul_f32_e32 v111, v111, v111
	v_mul_f32_e32 v112, v112, v112
	v_mul_f32_e32 v113, v113, v113
	v_mul_f32_e32 v106, v106, v106
	v_mul_f32_e32 v107, v107, v107
	v_mul_f32_e32 v108, v108, v108
	v_mul_f32_e32 v109, v109, v109
	v_cvt_pk_bf16_f32 v110, v110, v111
	v_cvt_pk_bf16_f32 v111, v112, v113
	v_cvt_pk_bf16_f32 v112, v106, v107
	v_cvt_pk_bf16_f32 v113, v108, v109
	ds_bpermute_b32 v110, v148, v110
	ds_bpermute_b32 v111, v148, v111
	ds_bpermute_b32 v112, v148, v112
	ds_bpermute_b32 v113, v148, v113
	v_mov_b32_e32 v106, 0
	v_mov_b32_e32 v107, 0
	v_mov_b32_e32 v108, 0
	v_mov_b32_e32 v109, 0
	v_mov_b32_e32 v126, 0
	v_mov_b32_e32 v127, 0
	v_mov_b32_e32 v128, 0
	v_mov_b32_e32 v129, 0
	s_waitcnt lgkmcnt(4)
	global_store_dwordx4 v[142:143], v[118:121], off offset:256
	v_lshl_add_u64 v[142:143], v[142:143], 0, s[98:99]
	v_max_f32_e32 v102, 0, v102
	v_max_f32_e32 v103, 0, v103
	v_max_f32_e32 v104, 0, v104
	v_max_f32_e32 v105, 0, v105
	v_max_f32_e32 v98, 0, v98
	v_max_f32_e32 v99, 0, v99
	v_max_f32_e32 v100, 0, v100
	v_max_f32_e32 v101, 0, v101
	v_mul_f32_e32 v102, v102, v102
	v_mul_f32_e32 v103, v103, v103
	v_mul_f32_e32 v104, v104, v104
	v_mul_f32_e32 v105, v105, v105
	v_mul_f32_e32 v98, v98, v98
	v_mul_f32_e32 v99, v99, v99
	v_mul_f32_e32 v100, v100, v100
	v_mul_f32_e32 v101, v101, v101
	v_cvt_pk_bf16_f32 v102, v102, v103
	v_cvt_pk_bf16_f32 v103, v104, v105
	v_cvt_pk_bf16_f32 v104, v98, v99
	v_cvt_pk_bf16_f32 v105, v100, v101
	ds_bpermute_b32 v102, v148, v102
	ds_bpermute_b32 v103, v148, v103
	ds_bpermute_b32 v104, v148, v104
	ds_bpermute_b32 v105, v148, v105
	v_mov_b32_e32 v98, 0
	v_mov_b32_e32 v99, 0
	v_mov_b32_e32 v100, 0
	v_mov_b32_e32 v101, 0
	v_mov_b32_e32 v118, 0
	v_mov_b32_e32 v119, 0
	v_mov_b32_e32 v120, 0
	v_mov_b32_e32 v121, 0
	s_waitcnt lgkmcnt(4)
	global_store_dwordx4 v[142:143], v[110:113], off
	v_max_f32_e32 v94, 0, v94
	v_max_f32_e32 v95, 0, v95
	v_max_f32_e32 v96, 0, v96
	v_max_f32_e32 v97, 0, v97
	v_max_f32_e32 v90, 0, v90
	v_max_f32_e32 v91, 0, v91
	v_max_f32_e32 v92, 0, v92
	v_max_f32_e32 v93, 0, v93
	v_mul_f32_e32 v94, v94, v94
	v_mul_f32_e32 v95, v95, v95
	v_mul_f32_e32 v96, v96, v96
	v_mul_f32_e32 v97, v97, v97
	v_mul_f32_e32 v90, v90, v90
	v_mul_f32_e32 v91, v91, v91
	v_mul_f32_e32 v92, v92, v92
	v_mul_f32_e32 v93, v93, v93
	v_cvt_pk_bf16_f32 v94, v94, v95
	v_cvt_pk_bf16_f32 v95, v96, v97
	v_cvt_pk_bf16_f32 v96, v90, v91
	v_cvt_pk_bf16_f32 v97, v92, v93
	ds_bpermute_b32 v94, v148, v94
	ds_bpermute_b32 v95, v148, v95
	ds_bpermute_b32 v96, v148, v96
	ds_bpermute_b32 v97, v148, v97
	v_mov_b32_e32 v90, 0
	v_mov_b32_e32 v91, 0
	v_mov_b32_e32 v92, 0
	v_mov_b32_e32 v93, 0
	v_mov_b32_e32 v110, 0
	v_mov_b32_e32 v111, 0
	v_mov_b32_e32 v112, 0
	v_mov_b32_e32 v113, 0
	s_waitcnt lgkmcnt(4)
	global_store_dwordx4 v[142:143], v[102:105], off offset:256
	v_lshl_add_u64 v[142:143], v[142:143], 0, s[98:99]
	v_max_f32_e32 v86, 0, v86
	v_max_f32_e32 v87, 0, v87
	v_max_f32_e32 v88, 0, v88
	v_max_f32_e32 v89, 0, v89
	v_max_f32_e32 v82, 0, v82
	v_max_f32_e32 v83, 0, v83
	v_max_f32_e32 v84, 0, v84
	v_max_f32_e32 v85, 0, v85
	v_mul_f32_e32 v86, v86, v86
	v_mul_f32_e32 v87, v87, v87
	v_mul_f32_e32 v88, v88, v88
	v_mul_f32_e32 v89, v89, v89
	v_mul_f32_e32 v82, v82, v82
	v_mul_f32_e32 v83, v83, v83
	v_mul_f32_e32 v84, v84, v84
	v_mul_f32_e32 v85, v85, v85
	v_cvt_pk_bf16_f32 v86, v86, v87
	v_cvt_pk_bf16_f32 v87, v88, v89
	v_cvt_pk_bf16_f32 v88, v82, v83
	v_cvt_pk_bf16_f32 v89, v84, v85
	ds_bpermute_b32 v86, v148, v86
	ds_bpermute_b32 v87, v148, v87
	ds_bpermute_b32 v88, v148, v88
	ds_bpermute_b32 v89, v148, v89
	v_mov_b32_e32 v82, 0
	v_mov_b32_e32 v83, 0
	v_mov_b32_e32 v84, 0
	v_mov_b32_e32 v85, 0
	v_mov_b32_e32 v102, 0
	v_mov_b32_e32 v103, 0
	v_mov_b32_e32 v104, 0
	v_mov_b32_e32 v105, 0
	s_waitcnt lgkmcnt(4)
	global_store_dwordx4 v[142:143], v[94:97], off
	v_max_f32_e32 v78, 0, v78
	v_max_f32_e32 v79, 0, v79
	v_max_f32_e32 v80, 0, v80
	v_max_f32_e32 v81, 0, v81
	v_max_f32_e32 v74, 0, v74
	v_max_f32_e32 v75, 0, v75
	v_max_f32_e32 v76, 0, v76
	v_max_f32_e32 v77, 0, v77
	v_mul_f32_e32 v78, v78, v78
	v_mul_f32_e32 v79, v79, v79
	v_mul_f32_e32 v80, v80, v80
	v_mul_f32_e32 v81, v81, v81
	v_mul_f32_e32 v74, v74, v74
	v_mul_f32_e32 v75, v75, v75
	v_mul_f32_e32 v76, v76, v76
	v_mul_f32_e32 v77, v77, v77
	v_cvt_pk_bf16_f32 v78, v78, v79
	v_cvt_pk_bf16_f32 v79, v80, v81
	v_cvt_pk_bf16_f32 v80, v74, v75
	v_cvt_pk_bf16_f32 v81, v76, v77
	ds_bpermute_b32 v78, v148, v78
	ds_bpermute_b32 v79, v148, v79
	ds_bpermute_b32 v80, v148, v80
	ds_bpermute_b32 v81, v148, v81
	v_mov_b32_e32 v74, 0
	v_mov_b32_e32 v75, 0
	v_mov_b32_e32 v76, 0
	v_mov_b32_e32 v77, 0
	v_mov_b32_e32 v94, 0
	v_mov_b32_e32 v95, 0
	v_mov_b32_e32 v96, 0
	v_mov_b32_e32 v97, 0
	s_waitcnt lgkmcnt(4)
	global_store_dwordx4 v[142:143], v[86:89], off offset:256
	v_lshl_add_u64 v[142:143], v[142:143], 0, s[98:99]
	v_max_f32_e32 v70, 0, v70
	v_max_f32_e32 v71, 0, v71
	v_max_f32_e32 v72, 0, v72
	v_max_f32_e32 v73, 0, v73
	v_max_f32_e32 v66, 0, v66
	v_max_f32_e32 v67, 0, v67
	v_max_f32_e32 v68, 0, v68
	v_max_f32_e32 v69, 0, v69
	v_mul_f32_e32 v70, v70, v70
	v_mul_f32_e32 v71, v71, v71
	v_mul_f32_e32 v72, v72, v72
	v_mul_f32_e32 v73, v73, v73
	v_mul_f32_e32 v66, v66, v66
	v_mul_f32_e32 v67, v67, v67
	v_mul_f32_e32 v68, v68, v68
	v_mul_f32_e32 v69, v69, v69
	v_cvt_pk_bf16_f32 v70, v70, v71
	v_cvt_pk_bf16_f32 v71, v72, v73
	v_cvt_pk_bf16_f32 v72, v66, v67
	v_cvt_pk_bf16_f32 v73, v68, v69
	ds_bpermute_b32 v70, v148, v70
	ds_bpermute_b32 v71, v148, v71
	ds_bpermute_b32 v72, v148, v72
	ds_bpermute_b32 v73, v148, v73
	v_mov_b32_e32 v66, 0
	v_mov_b32_e32 v67, 0
	v_mov_b32_e32 v68, 0
	v_mov_b32_e32 v69, 0
	v_mov_b32_e32 v86, 0
	v_mov_b32_e32 v87, 0
	v_mov_b32_e32 v88, 0
	v_mov_b32_e32 v89, 0
	s_waitcnt lgkmcnt(4)
	global_store_dwordx4 v[142:143], v[78:81], off
	v_max_f32_e32 v62, 0, v62
	v_max_f32_e32 v63, 0, v63
	v_max_f32_e32 v64, 0, v64
	v_max_f32_e32 v65, 0, v65
	v_max_f32_e32 v58, 0, v58
	v_max_f32_e32 v59, 0, v59
	v_max_f32_e32 v60, 0, v60
	v_max_f32_e32 v61, 0, v61
	v_mul_f32_e32 v62, v62, v62
	v_mul_f32_e32 v63, v63, v63
	v_mul_f32_e32 v64, v64, v64
	v_mul_f32_e32 v65, v65, v65
	v_mul_f32_e32 v58, v58, v58
	v_mul_f32_e32 v59, v59, v59
	v_mul_f32_e32 v60, v60, v60
	v_mul_f32_e32 v61, v61, v61
	v_cvt_pk_bf16_f32 v62, v62, v63
	v_cvt_pk_bf16_f32 v63, v64, v65
	v_cvt_pk_bf16_f32 v64, v58, v59
	v_cvt_pk_bf16_f32 v65, v60, v61
	ds_bpermute_b32 v62, v148, v62
	ds_bpermute_b32 v63, v148, v63
	ds_bpermute_b32 v64, v148, v64
	ds_bpermute_b32 v65, v148, v65
	v_mov_b32_e32 v58, 0
	v_mov_b32_e32 v59, 0
	v_mov_b32_e32 v60, 0
	v_mov_b32_e32 v61, 0
	v_mov_b32_e32 v78, 0
	v_mov_b32_e32 v79, 0
	v_mov_b32_e32 v80, 0
	v_mov_b32_e32 v81, 0
	s_waitcnt lgkmcnt(4)
	global_store_dwordx4 v[142:143], v[70:73], off offset:256
	v_lshl_add_u64 v[142:143], v[142:143], 0, s[100:101]
	v_max_f32_e32 v54, 0, v54
	v_max_f32_e32 v55, 0, v55
	v_max_f32_e32 v56, 0, v56
	v_max_f32_e32 v57, 0, v57
	v_max_f32_e32 v50, 0, v50
	v_max_f32_e32 v51, 0, v51
	v_max_f32_e32 v52, 0, v52
	v_max_f32_e32 v53, 0, v53
	v_mul_f32_e32 v54, v54, v54
	v_mul_f32_e32 v55, v55, v55
	v_mul_f32_e32 v56, v56, v56
	v_mul_f32_e32 v57, v57, v57
	v_mul_f32_e32 v50, v50, v50
	v_mul_f32_e32 v51, v51, v51
	v_mul_f32_e32 v52, v52, v52
	v_mul_f32_e32 v53, v53, v53
	v_cvt_pk_bf16_f32 v54, v54, v55
	v_cvt_pk_bf16_f32 v55, v56, v57
	v_cvt_pk_bf16_f32 v56, v50, v51
	v_cvt_pk_bf16_f32 v57, v52, v53
	ds_bpermute_b32 v54, v148, v54
	ds_bpermute_b32 v55, v148, v55
	ds_bpermute_b32 v56, v148, v56
	ds_bpermute_b32 v57, v148, v57
	v_mov_b32_e32 v50, 0
	v_mov_b32_e32 v51, 0
	v_mov_b32_e32 v52, 0
	v_mov_b32_e32 v53, 0
	v_mov_b32_e32 v70, 0
	v_mov_b32_e32 v71, 0
	v_mov_b32_e32 v72, 0
	v_mov_b32_e32 v73, 0
	s_waitcnt lgkmcnt(4)
	global_store_dwordx4 v[142:143], v[62:65], off
	v_max_f32_e32 v46, 0, v46
	v_max_f32_e32 v47, 0, v47
	v_max_f32_e32 v48, 0, v48
	v_max_f32_e32 v49, 0, v49
	v_max_f32_e32 v42, 0, v42
	v_max_f32_e32 v43, 0, v43
	v_max_f32_e32 v44, 0, v44
	v_max_f32_e32 v45, 0, v45
	v_mul_f32_e32 v46, v46, v46
	v_mul_f32_e32 v47, v47, v47
	v_mul_f32_e32 v48, v48, v48
	v_mul_f32_e32 v49, v49, v49
	v_mul_f32_e32 v42, v42, v42
	v_mul_f32_e32 v43, v43, v43
	v_mul_f32_e32 v44, v44, v44
	v_mul_f32_e32 v45, v45, v45
	v_cvt_pk_bf16_f32 v46, v46, v47
	v_cvt_pk_bf16_f32 v47, v48, v49
	v_cvt_pk_bf16_f32 v48, v42, v43
	v_cvt_pk_bf16_f32 v49, v44, v45
	ds_bpermute_b32 v46, v148, v46
	ds_bpermute_b32 v47, v148, v47
	ds_bpermute_b32 v48, v148, v48
	ds_bpermute_b32 v49, v148, v49
	v_mov_b32_e32 v42, 0
	v_mov_b32_e32 v43, 0
	v_mov_b32_e32 v44, 0
	v_mov_b32_e32 v45, 0
	v_mov_b32_e32 v62, 0
	v_mov_b32_e32 v63, 0
	v_mov_b32_e32 v64, 0
	v_mov_b32_e32 v65, 0
	s_waitcnt lgkmcnt(4)
	global_store_dwordx4 v[142:143], v[54:57], off offset:256
	v_lshl_add_u64 v[142:143], v[142:143], 0, s[98:99]
	v_max_f32_e32 v38, 0, v38
	v_max_f32_e32 v39, 0, v39
	v_max_f32_e32 v40, 0, v40
	v_max_f32_e32 v41, 0, v41
	v_max_f32_e32 v34, 0, v34
	v_max_f32_e32 v35, 0, v35
	v_max_f32_e32 v36, 0, v36
	v_max_f32_e32 v37, 0, v37
	v_mul_f32_e32 v38, v38, v38
	v_mul_f32_e32 v39, v39, v39
	v_mul_f32_e32 v40, v40, v40
	v_mul_f32_e32 v41, v41, v41
	v_mul_f32_e32 v34, v34, v34
	v_mul_f32_e32 v35, v35, v35
	v_mul_f32_e32 v36, v36, v36
	v_mul_f32_e32 v37, v37, v37
	v_cvt_pk_bf16_f32 v38, v38, v39
	v_cvt_pk_bf16_f32 v39, v40, v41
	v_cvt_pk_bf16_f32 v40, v34, v35
	v_cvt_pk_bf16_f32 v41, v36, v37
	ds_bpermute_b32 v38, v148, v38
	ds_bpermute_b32 v39, v148, v39
	ds_bpermute_b32 v40, v148, v40
	ds_bpermute_b32 v41, v148, v41
	v_mov_b32_e32 v34, 0
	v_mov_b32_e32 v35, 0
	v_mov_b32_e32 v36, 0
	v_mov_b32_e32 v37, 0
	v_mov_b32_e32 v54, 0
	v_mov_b32_e32 v55, 0
	v_mov_b32_e32 v56, 0
	v_mov_b32_e32 v57, 0
	s_waitcnt lgkmcnt(4)
	global_store_dwordx4 v[142:143], v[46:49], off
	v_max_f32_e32 v30, 0, v30
	v_max_f32_e32 v31, 0, v31
	v_max_f32_e32 v32, 0, v32
	v_max_f32_e32 v33, 0, v33
	v_max_f32_e32 v26, 0, v26
	v_max_f32_e32 v27, 0, v27
	v_max_f32_e32 v28, 0, v28
	v_max_f32_e32 v29, 0, v29
	v_mul_f32_e32 v30, v30, v30
	v_mul_f32_e32 v31, v31, v31
	v_mul_f32_e32 v32, v32, v32
	v_mul_f32_e32 v33, v33, v33
	v_mul_f32_e32 v26, v26, v26
	v_mul_f32_e32 v27, v27, v27
	v_mul_f32_e32 v28, v28, v28
	v_mul_f32_e32 v29, v29, v29
	v_cvt_pk_bf16_f32 v30, v30, v31
	v_cvt_pk_bf16_f32 v31, v32, v33
	v_cvt_pk_bf16_f32 v32, v26, v27
	v_cvt_pk_bf16_f32 v33, v28, v29
	ds_bpermute_b32 v30, v148, v30
	ds_bpermute_b32 v31, v148, v31
	ds_bpermute_b32 v32, v148, v32
	ds_bpermute_b32 v33, v148, v33
	v_mov_b32_e32 v26, 0
	v_mov_b32_e32 v27, 0
	v_mov_b32_e32 v28, 0
	v_mov_b32_e32 v29, 0
	v_mov_b32_e32 v46, 0
	v_mov_b32_e32 v47, 0
	v_mov_b32_e32 v48, 0
	v_mov_b32_e32 v49, 0
	s_waitcnt lgkmcnt(4)
	global_store_dwordx4 v[142:143], v[38:41], off offset:256
	v_lshl_add_u64 v[142:143], v[142:143], 0, s[98:99]
	v_max_f32_e32 v22, 0, v22
	v_max_f32_e32 v23, 0, v23
	v_max_f32_e32 v24, 0, v24
	v_max_f32_e32 v25, 0, v25
	v_max_f32_e32 v18, 0, v18
	v_max_f32_e32 v19, 0, v19
	v_max_f32_e32 v20, 0, v20
	v_max_f32_e32 v21, 0, v21
	v_mul_f32_e32 v22, v22, v22
	v_mul_f32_e32 v23, v23, v23
	v_mul_f32_e32 v24, v24, v24
	v_mul_f32_e32 v25, v25, v25
	v_mul_f32_e32 v18, v18, v18
	v_mul_f32_e32 v19, v19, v19
	v_mul_f32_e32 v20, v20, v20
	v_mul_f32_e32 v21, v21, v21
	v_cvt_pk_bf16_f32 v22, v22, v23
	v_cvt_pk_bf16_f32 v23, v24, v25
	v_cvt_pk_bf16_f32 v24, v18, v19
	v_cvt_pk_bf16_f32 v25, v20, v21
	ds_bpermute_b32 v22, v148, v22
	ds_bpermute_b32 v23, v148, v23
	ds_bpermute_b32 v24, v148, v24
	ds_bpermute_b32 v25, v148, v25
	v_mov_b32_e32 v18, 0
	v_mov_b32_e32 v19, 0
	v_mov_b32_e32 v20, 0
	v_mov_b32_e32 v21, 0
	v_mov_b32_e32 v38, 0
	v_mov_b32_e32 v39, 0
	v_mov_b32_e32 v40, 0
	v_mov_b32_e32 v41, 0
	s_waitcnt lgkmcnt(4)
	global_store_dwordx4 v[142:143], v[30:33], off
	v_max_f32_e32 v14, 0, v14
	v_max_f32_e32 v15, 0, v15
	v_max_f32_e32 v16, 0, v16
	v_max_f32_e32 v17, 0, v17
	v_max_f32_e32 v10, 0, v10
	v_max_f32_e32 v11, 0, v11
	v_max_f32_e32 v12, 0, v12
	v_max_f32_e32 v13, 0, v13
	v_mul_f32_e32 v14, v14, v14
	v_mul_f32_e32 v15, v15, v15
	v_mul_f32_e32 v16, v16, v16
	v_mul_f32_e32 v17, v17, v17
	v_mul_f32_e32 v10, v10, v10
	v_mul_f32_e32 v11, v11, v11
	v_mul_f32_e32 v12, v12, v12
	v_mul_f32_e32 v13, v13, v13
	v_cvt_pk_bf16_f32 v14, v14, v15
	v_cvt_pk_bf16_f32 v15, v16, v17
	v_cvt_pk_bf16_f32 v16, v10, v11
	v_cvt_pk_bf16_f32 v17, v12, v13
	ds_bpermute_b32 v14, v148, v14
	ds_bpermute_b32 v15, v148, v15
	ds_bpermute_b32 v16, v148, v16
	ds_bpermute_b32 v17, v148, v17
	v_mov_b32_e32 v10, 0
	v_mov_b32_e32 v11, 0
	v_mov_b32_e32 v12, 0
	v_mov_b32_e32 v13, 0
	v_mov_b32_e32 v30, 0
	v_mov_b32_e32 v31, 0
	v_mov_b32_e32 v32, 0
	v_mov_b32_e32 v33, 0
	s_waitcnt lgkmcnt(4)
	global_store_dwordx4 v[142:143], v[22:25], off offset:256
	v_lshl_add_u64 v[142:143], v[142:143], 0, s[98:99]
	v_max_f32_e32 v6, 0, v6
	v_max_f32_e32 v7, 0, v7
	v_max_f32_e32 v8, 0, v8
	v_max_f32_e32 v9, 0, v9
	v_max_f32_e32 v2, 0, v2
	v_max_f32_e32 v3, 0, v3
	v_max_f32_e32 v4, 0, v4
	v_max_f32_e32 v5, 0, v5
	v_mul_f32_e32 v6, v6, v6
	v_mul_f32_e32 v7, v7, v7
	v_mul_f32_e32 v8, v8, v8
	v_mul_f32_e32 v9, v9, v9
	v_mul_f32_e32 v2, v2, v2
	v_mul_f32_e32 v3, v3, v3
	v_mul_f32_e32 v4, v4, v4
	v_mul_f32_e32 v5, v5, v5
	v_cvt_pk_bf16_f32 v6, v6, v7
	v_cvt_pk_bf16_f32 v7, v8, v9
	v_cvt_pk_bf16_f32 v8, v2, v3
	v_cvt_pk_bf16_f32 v9, v4, v5
	ds_bpermute_b32 v6, v148, v6
	ds_bpermute_b32 v7, v148, v7
	ds_bpermute_b32 v8, v148, v8
	ds_bpermute_b32 v9, v148, v9
	v_mov_b32_e32 v2, 0
	v_mov_b32_e32 v3, 0
	v_mov_b32_e32 v4, 0
	v_mov_b32_e32 v5, 0
	v_mov_b32_e32 v22, 0
	v_mov_b32_e32 v23, 0
	v_mov_b32_e32 v24, 0
	v_mov_b32_e32 v25, 0
	s_waitcnt lgkmcnt(4)
	global_store_dwordx4 v[142:143], v[14:17], off
	s_waitcnt lgkmcnt(0)
	global_store_dwordx4 v[142:143], v[6:9], off offset:256
	v_mov_b32_e32 v14, 0
	v_mov_b32_e32 v15, 0
	v_mov_b32_e32 v16, 0
	v_mov_b32_e32 v17, 0
	s_nop 1
	v_mov_b32_e32 v6, 0
	v_mov_b32_e32 v7, 0
	v_mov_b32_e32 v8, 0
	v_mov_b32_e32 v9, 0
	s_mov_b64 s[36:37], 0x100000
	s_andn2_b64 vcc, exec, s[4:5]
	s_mov_b64 s[4:5], -1
	s_cbranch_vccnz .LBB0_1877
	s_andn2_b64 vcc, exec, s[8:9]
	s_cbranch_vccnz .LBB0_1876
	s_barrier
	s_branch .LBB0_1876
